# speedup vs baseline: 1.0296x; 1.0015x over previous
.LBB0_37:
	s_or_b64 exec, exec, s[14:15]
	v_readfirstlane_b32 s94, v0
	s_lshr_b32 s94, s94, 6
	s_cmp_lg_u32 s94, 1
	s_cbranch_scc1 .Llpt_done
	s_add_i32 s95, s33, 1
	s_ashr_i32 s95, s95, 1
	v_add_u32_e32 v100, 16, v3
	v_add_u32_e32 v101, 0x50, v3
	v_lshlrev_b32_e32 v102, 3, v100
	v_lshlrev_b32_e32 v103, 3, v101
	v_add_u32_e32 v102, 0x1dd00, v102
	v_add_u32_e32 v103, 0x1dd00, v103
	ds_read_b64 v[104:105], v102
	ds_read_b64 v[106:107], v103
	v_mov_b32_e32 v110, 0x26dd0
	s_waitcnt lgkmcnt(0)
	v_add_u32_e32 v104, v104, v105
	v_add_u32_e32 v106, v106, v107
	v_add_u32_e32 v104, 15, v104
	v_add_u32_e32 v106, 15, v106
	v_lshrrev_b32_e32 v104, 4, v104
	v_lshrrev_b32_e32 v106, 4, v106
	v_max_u32_e32 v104, 1, v104
	v_max_u32_e32 v106, 1, v106
	v_min_u32_e32 v104, 7, v104
	v_min_u32_e32 v106, 7, v106
	v_cmp_gt_i32_e32 vcc, s95, v100
	s_nop 1
	v_cndmask_b32_e32 v104, 0, v104, vcc
	v_cmp_gt_i32_e32 vcc, s95, v101
	s_nop 1
	v_cndmask_b32_e32 v106, 0, v106, vcc
	s_mov_b32 s94, 16
	v_cmp_eq_u32_e64 s[34:35], 7, v104
	v_cmp_eq_u32_e64 s[36:37], 7, v106
	s_bcnt1_i32_b64 s73, s[34:35]
	s_nop 0
	v_mbcnt_lo_u32_b32 v108, s34, 0
	v_mbcnt_hi_u32_b32 v108, s35, v108
	v_add_u32_e32 v108, s94, v108
	s_add_i32 s94, s94, s73
	v_mbcnt_lo_u32_b32 v109, s36, 0
	v_mbcnt_hi_u32_b32 v109, s37, v109
	v_add_u32_e32 v109, s94, v109
	s_bcnt1_i32_b64 s73, s[36:37]
	s_add_i32 s94, s94, s73
	v_lshl_add_u32 v108, v108, 2, v110
	v_lshl_add_u32 v109, v109, 2, v110
	s_mov_b64 exec, s[34:35]
	ds_write_b32 v108, v100
	s_mov_b64 exec, s[36:37]
	ds_write_b32 v109, v101
	s_mov_b64 exec, -1
	v_cmp_eq_u32_e64 s[34:35], 6, v104
	v_cmp_eq_u32_e64 s[36:37], 6, v106
	s_bcnt1_i32_b64 s73, s[34:35]
	s_nop 0
	v_mbcnt_lo_u32_b32 v108, s34, 0
	v_mbcnt_hi_u32_b32 v108, s35, v108
	v_add_u32_e32 v108, s94, v108
	s_add_i32 s94, s94, s73
	v_mbcnt_lo_u32_b32 v109, s36, 0
	v_mbcnt_hi_u32_b32 v109, s37, v109
	v_add_u32_e32 v109, s94, v109
	s_bcnt1_i32_b64 s73, s[36:37]
	s_add_i32 s94, s94, s73
	v_lshl_add_u32 v108, v108, 2, v110
	v_lshl_add_u32 v109, v109, 2, v110
	s_mov_b64 exec, s[34:35]
	ds_write_b32 v108, v100
	s_mov_b64 exec, s[36:37]
	ds_write_b32 v109, v101
	s_mov_b64 exec, -1
	v_cmp_eq_u32_e64 s[34:35], 5, v104
	v_cmp_eq_u32_e64 s[36:37], 5, v106
	s_bcnt1_i32_b64 s73, s[34:35]
	s_nop 0
	v_mbcnt_lo_u32_b32 v108, s34, 0
	v_mbcnt_hi_u32_b32 v108, s35, v108
	v_add_u32_e32 v108, s94, v108
	s_add_i32 s94, s94, s73
	v_mbcnt_lo_u32_b32 v109, s36, 0
	v_mbcnt_hi_u32_b32 v109, s37, v109
	v_add_u32_e32 v109, s94, v109
	s_bcnt1_i32_b64 s73, s[36:37]
	s_add_i32 s94, s94, s73
	v_lshl_add_u32 v108, v108, 2, v110
	v_lshl_add_u32 v109, v109, 2, v110
	s_mov_b64 exec, s[34:35]
	ds_write_b32 v108, v100
	s_mov_b64 exec, s[36:37]
	ds_write_b32 v109, v101
	s_mov_b64 exec, -1
	v_cmp_eq_u32_e64 s[34:35], 4, v104
	v_cmp_eq_u32_e64 s[36:37], 4, v106
	s_bcnt1_i32_b64 s73, s[34:35]
	s_nop 0
	v_mbcnt_lo_u32_b32 v108, s34, 0
	v_mbcnt_hi_u32_b32 v108, s35, v108
	v_add_u32_e32 v108, s94, v108
	s_add_i32 s94, s94, s73
	v_mbcnt_lo_u32_b32 v109, s36, 0
	v_mbcnt_hi_u32_b32 v109, s37, v109
	v_add_u32_e32 v109, s94, v109
	s_bcnt1_i32_b64 s73, s[36:37]
	s_add_i32 s94, s94, s73
	v_lshl_add_u32 v108, v108, 2, v110
	v_lshl_add_u32 v109, v109, 2, v110
	s_mov_b64 exec, s[34:35]
	ds_write_b32 v108, v100
	s_mov_b64 exec, s[36:37]
	ds_write_b32 v109, v101
	s_mov_b64 exec, -1
	v_cmp_eq_u32_e64 s[34:35], 3, v104
	v_cmp_eq_u32_e64 s[36:37], 3, v106
	s_bcnt1_i32_b64 s73, s[34:35]
	s_nop 0
	v_mbcnt_lo_u32_b32 v108, s34, 0
	v_mbcnt_hi_u32_b32 v108, s35, v108
	v_add_u32_e32 v108, s94, v108
	s_add_i32 s94, s94, s73
	v_mbcnt_lo_u32_b32 v109, s36, 0
	v_mbcnt_hi_u32_b32 v109, s37, v109
	v_add_u32_e32 v109, s94, v109
	s_bcnt1_i32_b64 s73, s[36:37]
	s_add_i32 s94, s94, s73
	v_lshl_add_u32 v108, v108, 2, v110
	v_lshl_add_u32 v109, v109, 2, v110
	s_mov_b64 exec, s[34:35]
	ds_write_b32 v108, v100
	s_mov_b64 exec, s[36:37]
	ds_write_b32 v109, v101
	s_mov_b64 exec, -1
	v_cmp_eq_u32_e64 s[34:35], 2, v104
	v_cmp_eq_u32_e64 s[36:37], 2, v106
	s_bcnt1_i32_b64 s73, s[34:35]
	s_nop 0
	v_mbcnt_lo_u32_b32 v108, s34, 0
	v_mbcnt_hi_u32_b32 v108, s35, v108
	v_add_u32_e32 v108, s94, v108
	s_add_i32 s94, s94, s73
	v_mbcnt_lo_u32_b32 v109, s36, 0
	v_mbcnt_hi_u32_b32 v109, s37, v109
	v_add_u32_e32 v109, s94, v109
	s_bcnt1_i32_b64 s73, s[36:37]
	s_add_i32 s94, s94, s73
	v_lshl_add_u32 v108, v108, 2, v110
	v_lshl_add_u32 v109, v109, 2, v110
	s_mov_b64 exec, s[34:35]
	ds_write_b32 v108, v100
	s_mov_b64 exec, s[36:37]
	ds_write_b32 v109, v101
	s_mov_b64 exec, -1
	v_cmp_eq_u32_e64 s[34:35], 1, v104
	v_cmp_eq_u32_e64 s[36:37], 1, v106
	s_bcnt1_i32_b64 s73, s[34:35]
	s_nop 0
	v_mbcnt_lo_u32_b32 v108, s34, 0
	v_mbcnt_hi_u32_b32 v108, s35, v108
	v_add_u32_e32 v108, s94, v108
	s_add_i32 s94, s94, s73
	v_mbcnt_lo_u32_b32 v109, s36, 0
	v_mbcnt_hi_u32_b32 v109, s37, v109
	v_add_u32_e32 v109, s94, v109
	s_bcnt1_i32_b64 s73, s[36:37]
	s_add_i32 s94, s94, s73
	v_lshl_add_u32 v108, v108, 2, v110
	v_lshl_add_u32 v109, v109, 2, v110
	s_mov_b64 exec, s[34:35]
	ds_write_b32 v108, v100
	s_mov_b64 exec, s[36:37]
	ds_write_b32 v109, v101
	s_mov_b64 exec, -1

.LBB0_71:
	s_or_b64 exec, exec, s[0:1]
	s_add_i32 s0, s33, 1
	s_ashr_i32 s68, s0, 1
	v_readfirstlane_b32 s18, v4
	s_cmp_ge_i32 s18, s68
	s_cbranch_scc1 .Llpt_map1
	s_lshl_b32 s94, s18, 2
	s_add_i32 s94, s94, 0x26dd0
	v_mov_b32_e32 v117, s94
	ds_read_b32 v117, v117
	s_waitcnt lgkmcnt(0)
	v_readfirstlane_b32 s18, v117

.LBB0_81:
	s_or_b64 exec, exec, s[8:9]
	v_readfirstlane_b32 s0, v7
	s_cmp_ge_i32 s0, s68
	s_cbranch_scc1 .Llpt_map2
	s_lshl_b32 s94, s0, 2
	s_add_i32 s94, s94, 0x26dd0
	v_mov_b32_e32 v117, s94
	ds_read_b32 v117, v117
	s_waitcnt lgkmcnt(0)
	v_readfirstlane_b32 s0, v117

.LBB0_89:
	s_or_b64 exec, exec, s[8:9]
	v_mov_b32_e32 v3, 0
	v_lshlrev_b32_e32 v70, 4, v28
	s_and_saveexec_b64 s[60:61], vcc
	s_cbranch_execz .LBB0_118
	s_mov_b64 s[92:93], s[14:15]
	v_lshl_add_u64 v[22:23], s[12:13], 0, v[2:3]
	s_waitcnt vmcnt(0)
	v_cndmask_b32_e64 v55, -1, v4, s[0:1]
	s_movk_i32 s0, 0x880
	v_mov_b32_e32 v2, 0x1dd00
	v_mad_u32_u24 v4, v80, s0, v2
	v_lshlrev_b32_e32 v2, 1, v1
	v_mov_b32_e32 v27, v3
	v_mbcnt_hi_u32_b32 v2, -1, v29
	v_lshl_add_u64 v[72:73], v[22:23], 0, v[26:27]
	v_and_b32_e32 v23, 64, v2
	v_xor_b32_e32 v22, 16, v2
	v_add_u32_e32 v23, 64, v23
	v_cmp_lt_i32_e32 vcc, v22, v23
	v_lshlrev_b32_e32 v88, 2, v28
	v_and_b32_e32 v24, 7, v0
	v_cndmask_b32_e32 v22, v2, v22, vcc
	v_lshlrev_b32_e32 v90, 2, v22
	v_xor_b32_e32 v22, 32, v2
	v_cmp_lt_i32_e32 vcc, v22, v23
	s_mov_b32 s24, 0x10000
	v_cndmask_b32_e32 v2, v2, v22, vcc
	v_lshlrev_b32_e32 v91, 2, v2
	v_lshrrev_b32_e32 v2, 2, v79
	v_mul_u32_u24_e32 v22, 0x88, v79
	v_add3_u32 v92, v4, v22, v1
	v_or_b32_e32 v2, v88, v2
	v_lshlrev_b32_e32 v22, 3, v0
	v_mul_u32_u24_e32 v2, 0x88, v2
	v_and_b32_e32 v22, 24, v22
	v_add3_u32 v93, v4, v2, v22
	v_lshlrev_b32_e32 v2, 5, v24
	v_or3_b32 v78, v2, v1, s24
	v_bfe_u32 v2, v0, 1, 2
	v_lshrrev_b32_e32 v89, 3, v79
	v_cmp_eq_u32_e64 s[6:7], 4, v24
	v_cmp_eq_u32_e64 s[8:9], 3, v24
	v_cmp_eq_u32_e64 s[10:11], 2, v24
	v_cmp_eq_u32_e64 s[12:13], 1, v24
	v_cmp_eq_u32_e64 s[14:15], 0, v24
	v_cmp_eq_u32_e64 s[16:17], 7, v24
	v_cmp_eq_u32_e64 s[18:19], 6, v24
	v_cmp_eq_u32_e64 s[20:21], 5, v24
	v_cmp_eq_u32_e64 s[22:23], 0, v2
	v_cmp_eq_u32_e64 s[24:25], 1, v2
	v_cmp_eq_u32_e64 s[26:27], 2, v2
	v_cmp_eq_u32_e64 s[28:29], 3, v2
	s_and_b64 s[22:23], s[22:23], s[4:5]
	s_and_b64 s[24:25], s[24:25], s[4:5]
	s_and_b64 s[26:27], s[26:27], s[4:5]
	s_and_b64 s[28:29], s[28:29], s[4:5]
	v_mov_b32_e32 v71, 0xf149f2ca
	s_mov_b64 s[62:63], 0
	s_mov_b32 s69, 0xf149f2ca
	s_mov_b32 s70, 0xefa18f08
	s_mov_b32 s71, 0x41000000
	s_movk_i32 s72, 0x110
	s_mov_b32 s77, 0x26500
	s_mov_b32 s73, 0x2650c
	s_mov_b32 s80, -1
	s_mov_b32 s81, 0
	s_mov_b32 s82, 0
	s_mov_b32 s83, 0x7fffffff
	s_mov_b64 s[84:85], 0
	v_mov_b32_e32 v100, 0
	v_mov_b32_e32 v4, 0
	v_mov_b32_e32 v103, 0xf149f2ca
	v_mov_b32_e32 v46, v3
	v_mov_b32_e32 v47, v3
	v_mov_b32_e32 v48, v3
	v_mov_b32_e32 v49, v3
	v_mov_b32_e32 v50, v3
	v_mov_b32_e32 v51, v3
	v_mov_b32_e32 v52, v3
	v_mov_b32_e32 v53, v3
	v_mov_b32_e32 v38, v3
	v_mov_b32_e32 v39, v3
	v_mov_b32_e32 v40, v3
	v_mov_b32_e32 v41, v3
	v_mov_b32_e32 v42, v3
	v_mov_b32_e32 v43, v3
	v_mov_b32_e32 v44, v3
	v_mov_b32_e32 v45, v3
	v_mov_b32_e32 v30, v3
	v_mov_b32_e32 v31, v3
	v_mov_b32_e32 v32, v3
	v_mov_b32_e32 v33, v3
	v_mov_b32_e32 v34, v3
	v_mov_b32_e32 v35, v3
	v_mov_b32_e32 v36, v3
	v_mov_b32_e32 v37, v3
	v_mov_b32_e32 v22, v3
	v_mov_b32_e32 v23, v3
	v_mov_b32_e32 v24, v3
	v_mov_b32_e32 v25, v3
	v_mov_b32_e32 v26, v3
	v_mov_b32_e32 v28, v3
	v_mov_b32_e32 v29, v3
	v_readfirstlane_b32 s86, v80
	s_mov_b32 s87, 0
	v_readfirstlane_b32 s88, v99
	v_readfirstlane_b32 s89, v5
	v_readfirstlane_b32 s96, v54
	v_readfirstlane_b32 s97, v84
	v_readfirstlane_b32 s98, v85
	v_readfirstlane_b32 s99, v81
	v_readfirstlane_b32 s100, v83
	v_readfirstlane_b32 s101, v82
	v_mov_b32_e32 v84, v82
	s_cmp_ge_i32 s96, s68
	s_cselect_b32 s100, 0, s100
	s_branch .LBB0_95

.Lattn_skip:
	s_cmp_ge_i32 s86, s68
	s_cbranch_scc1 .LBB0_118
	s_mov_b32 s80, s86
	s_mov_b32 s81, s87
	s_mov_b32 s82, s89
	s_mov_b32 s83, s88
	s_mov_b64 s[84:85], s[90:91]
	s_mov_b32 s86, s96
	s_mov_b32 s87, s97
	s_mov_b32 s88, s100
	s_mov_b32 s89, s99
	s_waitcnt vmcnt(4)
	v_cndmask_b32_e64 v55, -1, v98, s[30:31]
	s_cmp_ge_i32 s96, s68
	s_cbranch_scc1 .LBB0_95
	s_add_i32 s97, s97, 1
	s_lshl_b32 s94, s97, 4
	s_cmp_lt_i32 s94, s100
	s_cbranch_scc1 .LBB0_95
	s_mov_b32 s97, 0
	s_waitcnt lgkmcnt(0)
	v_readfirstlane_b32 s96, v84
	v_mov_b32_e32 v2, 0x26b40
	v_mov_b32_e32 v104, 1
	s_mov_b64 exec, 1
	ds_add_rtn_u32 v104, v2, v104
	s_mov_b64 exec, -1
	s_cmp_ge_i32 s96, s68
	s_cbranch_scc1 .Lattn_c1inv
	s_lshl_b32 s94, s96, 1
	s_min_i32 s95, s94, s67
	s_lshl_b32 s95, s95, 3
	s_add_i32 s95, s95, 0x26500
	v_mov_b32_e32 v2, s95
	ds_read_b64 v[106:107], v2
	s_or_b32 s95, s94, 1
	s_min_i32 s74, s95, s67
	s_lshl_b32 s74, s74, 3
	s_add_i32 s74, s74, 0x26504
	v_mov_b32_e32 v2, s74
	ds_read_b32 v105, v2
	s_waitcnt lgkmcnt(0)
	v_readfirstlane_b32 s98, v106
	v_readfirstlane_b32 s99, v107
	v_readfirstlane_b32 s100, v105
	s_cmp_lt_i32 s95, s33
	s_cselect_b32 s100, s100, 0
	s_add_i32 s100, s100, s99
	s_branch .Lattn_map
.Lattn_c1inv:
	s_waitcnt lgkmcnt(0)
	s_mov_b32 s100, 0
	s_mov_b32 s98, 0
.Lattn_map:
	v_readfirstlane_b32 s101, v104
	s_nop 0
	v_mov_b32_e32 v84, s101
	s_cmp_ge_i32 s101, s68
	s_cbranch_scc1 .LBB0_95
	s_lshl_b32 s94, s101, 2
	s_add_i32 s94, s94, 0x26dd0
	v_mov_b32_e32 v2, s94
	ds_read_b32 v84, v2
	s_branch .LBB0_95

	.amdhsa_kernel _Z7k_attn3PKDF16_S0_PKiS2_PiPKDv8_DF16_PKfS6_S8_Pf
		.amdhsa_group_segment_fixed_size 159696
		.amdhsa_private_segment_fixed_size 0
		.amdhsa_kernarg_size 80
		.amdhsa_user_sgpr_count 2
		.amdhsa_user_sgpr_dispatch_ptr 0
		.amdhsa_user_sgpr_queue_ptr 0
		.amdhsa_user_sgpr_kernarg_segment_ptr 1
		.amdhsa_user_sgpr_dispatch_id 0
		.amdhsa_user_sgpr_kernarg_preload_length 0
		.amdhsa_user_sgpr_kernarg_preload_offset 0
		.amdhsa_user_sgpr_private_segment_size 0
		.amdhsa_uses_dynamic_stack 0
		.amdhsa_enable_private_segment 0
		.amdhsa_system_sgpr_workgroup_id_x 1
		.amdhsa_system_sgpr_workgroup_id_y 0
		.amdhsa_system_sgpr_workgroup_id_z 0
		.amdhsa_system_sgpr_workgroup_info 0
		.amdhsa_system_vgpr_workitem_id 0
		.amdhsa_next_free_vgpr 128
		.amdhsa_next_free_sgpr 102
		.amdhsa_accum_offset 128
		.amdhsa_reserve_vcc 1
		.amdhsa_float_round_mode_32 0
		.amdhsa_float_round_mode_16_64 0
		.amdhsa_float_denorm_mode_32 3
		.amdhsa_float_denorm_mode_16_64 3
		.amdhsa_dx10_clamp 1
		.amdhsa_ieee_mode 1
		.amdhsa_fp16_overflow 0
		.amdhsa_tg_split 0
		.amdhsa_exception_fp_ieee_invalid_op 0
		.amdhsa_exception_fp_denorm_src 0
		.amdhsa_exception_fp_ieee_div_zero 0
		.amdhsa_exception_fp_ieee_overflow 0
		.amdhsa_exception_fp_ieee_underflow 0
		.amdhsa_exception_fp_ieee_inexact 0
		.amdhsa_exception_int_div_zero 0
	.end_amdhsa_kernel

amdhsa.kernels:
  - .agpr_count:     0
    .args:
      - .actual_access:  read_only
        .address_space:  global
        .offset:         0
        .size:           8
        .value_kind:     global_buffer
      - .actual_access:  read_only
        .address_space:  global
        .offset:         8
        .size:           8
        .value_kind:     global_buffer
      - .actual_access:  read_only
        .address_space:  global
        .offset:         16
        .size:           8
        .value_kind:     global_buffer
      - .actual_access:  read_only
        .address_space:  global
        .offset:         24
        .size:           8
        .value_kind:     global_buffer
      - .address_space:  global
        .offset:         32
        .size:           8
        .value_kind:     global_buffer
      - .actual_access:  read_only
        .address_space:  global
        .offset:         40
        .size:           8
        .value_kind:     global_buffer
      - .actual_access:  read_only
        .address_space:  global
        .offset:         48
        .size:           8
        .value_kind:     global_buffer
      - .actual_access:  read_only
        .address_space:  global
        .offset:         56
        .size:           8
        .value_kind:     global_buffer
      - .actual_access:  read_only
        .address_space:  global
        .offset:         64
        .size:           8
        .value_kind:     global_buffer
      - .actual_access:  write_only
        .address_space:  global
        .offset:         72
        .size:           8
        .value_kind:     global_buffer
    .group_segment_fixed_size: 159696
    .kernarg_segment_align: 8
    .kernarg_segment_size: 80
    .language:       OpenCL C
    .language_version:
      - 2
      - 0
    .max_flat_workgroup_size: 1024
    .name:           _Z7k_attn3PKDF16_S0_PKiS2_PiPKDv8_DF16_PKfS6_S8_Pf
    .private_segment_fixed_size: 0
    .sgpr_count:     79
    .sgpr_spill_count: 0
    .symbol:         _Z7k_attn3PKDF16_S0_PKiS2_PiPKDv8_DF16_PKfS6_S8_Pf.kd
    .uniform_work_group_size: 1
    .uses_dynamic_stack: false
    .vgpr_count:     128
    .vgpr_spill_count: 0
    .wavefront_size: 64
  - .agpr_count:     0
    .args:
      - .actual_access:  read_only
        .address_space:  global
        .offset:         0
        .size:           8
        .value_kind:     global_buffer
      - .actual_access:  write_only
        .address_space:  global
        .offset:         8
        .size:           8
        .value_kind:     global_buffer
      - .actual_access:  read_only
        .address_space:  global
        .offset:         16
        .size:           8
        .value_kind:     global_buffer
      - .actual_access:  read_only
        .address_space:  global
        .offset:         24
        .size:           8
        .value_kind:     global_buffer
      - .actual_access:  read_only
        .address_space:  global
        .offset:         32
        .size:           8
        .value_kind:     global_buffer
      - .actual_access:  read_only
        .address_space:  global
        .offset:         40
        .size:           8
        .value_kind:     global_buffer
      - .actual_access:  read_only
        .address_space:  global
        .offset:         48
        .size:           8
        .value_kind:     global_buffer
      - .actual_access:  read_only
        .address_space:  global
        .offset:         56
        .size:           8
        .value_kind:     global_buffer
      - .actual_access:  read_only
        .address_space:  global
        .offset:         64
        .size:           8
        .value_kind:     global_buffer
      - .actual_access:  write_only
        .address_space:  global
        .offset:         72
        .size:           8
        .value_kind:     global_buffer
      - .actual_access:  write_only
        .address_space:  global
        .offset:         80
        .size:           8
        .value_kind:     global_buffer
      - .actual_access:  write_only
        .address_space:  global
        .offset:         88
        .size:           8
        .value_kind:     global_buffer
      - .actual_access:  write_only
        .address_space:  global
        .offset:         96
        .size:           8
        .value_kind:     global_buffer
    .group_segment_fixed_size: 1024
    .kernarg_segment_align: 8
    .kernarg_segment_size: 104
    .language:       OpenCL C
    .language_version:
      - 2
      - 0
    .max_flat_workgroup_size: 512
    .name:           _Z4k_l1PK15HIP_vector_typeIiLj4EEPiPKfS5_S5_S5_S5_S5_S5_PDF16_PfS6_S6_
    .private_segment_fixed_size: 0
    .sgpr_count:     22
    .sgpr_spill_count: 0
    .symbol:         _Z4k_l1PK15HIP_vector_typeIiLj4EEPiPKfS5_S5_S5_S5_S5_S5_PDF16_PfS6_S6_.kd
    .uniform_work_group_size: 1
    .uses_dynamic_stack: false
    .vgpr_count:     24
    .vgpr_spill_count: 0
    .wavefront_size: 64
  - .agpr_count:     0
    .args:
      - .actual_access:  read_only
        .address_space:  global
        .offset:         0
        .size:           8
        .value_kind:     global_buffer
      - .actual_access:  read_only
        .address_space:  global
        .offset:         8
        .size:           8
        .value_kind:     global_buffer
      - .actual_access:  read_only
        .address_space:  global
        .offset:         16
        .size:           8
        .value_kind:     global_buffer
      - .actual_access:  write_only
        .address_space:  global
        .offset:         24
        .size:           8
        .value_kind:     global_buffer
      - .actual_access:  write_only
        .address_space:  global
        .offset:         32
        .size:           8
        .value_kind:     global_buffer
      - .actual_access:  read_only
        .address_space:  global
        .offset:         40
        .size:           8
        .value_kind:     global_buffer
      - .actual_access:  read_only
        .address_space:  global
        .offset:         48
        .size:           8
        .value_kind:     global_buffer
      - .actual_access:  read_only
        .address_space:  global
        .offset:         56
        .size:           8
        .value_kind:     global_buffer
      - .actual_access:  write_only
        .address_space:  global
        .offset:         64
        .size:           8
        .value_kind:     global_buffer
      - .actual_access:  write_only
        .address_space:  global
        .offset:         72
        .size:           8
        .value_kind:     global_buffer
    .group_segment_fixed_size: 53248
    .kernarg_segment_align: 8
    .kernarg_segment_size: 80
    .language:       OpenCL C
    .language_version:
      - 2
      - 0
    .max_flat_workgroup_size: 512
    .name:           _Z4k_l2PK15HIP_vector_typeIiLj4EES2_PKiPiS5_PKfPKDv8_DF16_S7_PDF16_SB_
    .private_segment_fixed_size: 0
    .sgpr_count:     34
    .sgpr_spill_count: 0
    .symbol:         _Z4k_l2PK15HIP_vector_typeIiLj4EES2_PKiPiS5_PKfPKDv8_DF16_S7_PDF16_SB_.kd
    .uniform_work_group_size: 1
    .uses_dynamic_stack: false
    .vgpr_count:     126
    .vgpr_spill_count: 0
    .wavefront_size: 64
